# speedup vs baseline: 1.0089x; 1.0089x over previous
_Z6k_normILb1EEvPKDF16_PKdPKfS5_Pvm:
	s_cmpk_gt_u32 s2, 0x30d
	s_cselect_b64 s[8:9], -1, 0
	s_load_dwordx4 s[4:7], s[0:1], 0x8
	s_load_dwordx2 s[10:11], s[0:1], 0x18
	s_and_b64 s[12:13], s[8:9], exec
	s_cselect_b32 s3, 0x1000, 0
	v_or_b32_e32 v1, s3, v0
	v_lshlrev_b32_e32 v1, 3, v1
	v_or_b32_e32 v10, 0x1000, v1
	s_waitcnt lgkmcnt(0)
	global_load_dwordx2 v[2:3], v1, s[4:5]
	global_load_dwordx2 v[4:5], v1, s[4:5] offset:2048
	global_load_dwordx2 v[6:7], v10, s[4:5]
	global_load_dwordx2 v[8:9], v10, s[4:5] offset:2048
	v_or_b32_e32 v18, 0x2000, v1
	v_or_b32_e32 v19, 0x3000, v1
	global_load_dwordx2 v[10:11], v18, s[4:5]
	global_load_dwordx2 v[12:13], v18, s[4:5] offset:2048
	global_load_dwordx2 v[14:15], v19, s[4:5]
	global_load_dwordx2 v[16:17], v19, s[4:5] offset:2048
	v_or_b32_e32 v26, 0x4000, v1
	v_or_b32_e32 v27, 0x5000, v1
	global_load_dwordx2 v[18:19], v26, s[4:5]
	global_load_dwordx2 v[20:21], v26, s[4:5] offset:2048
	global_load_dwordx2 v[22:23], v27, s[4:5]
	global_load_dwordx2 v[24:25], v27, s[4:5] offset:2048
	v_or_b32_e32 v34, 0x6000, v1
	v_or_b32_e32 v1, 0x7000, v1
	global_load_dwordx2 v[26:27], v34, s[4:5]
	global_load_dwordx2 v[28:29], v34, s[4:5] offset:2048
	global_load_dwordx2 v[30:31], v1, s[4:5]
	global_load_dwordx2 v[32:33], v1, s[4:5] offset:2048
	s_cselect_b32 s3, 0x100, 0
	v_or_b32_e32 v1, s3, v0
	v_lshlrev_b32_e32 v1, 2, v1
	global_load_dword v34, v1, s[6:7]
	global_load_dword v35, v1, s[10:11]
	s_mov_b32 s10, 0
	s_cselect_b32 s3, 0x3fffcf2, 0
	s_mov_b32 s11, 0x40e86a00
	s_add_i32 s3, s3, s2
	s_lshl_b32 s4, s3, 6
	s_mov_b32 s5, 0x800000
	v_lshrrev_b32_e32 v1, 5, v0
	s_add_i32 s12, s4, 64
	s_min_i32 s16, s12, 0xc350
	s_mov_b64 s[6:7], 0
	v_lshlrev_b32_e32 v36, 2, v0
	s_waitcnt vmcnt(17)
	v_add_f64 v[2:3], v[2:3], 0
	s_waitcnt vmcnt(16)
	v_add_f64 v[4:5], v[4:5], 0
	s_waitcnt vmcnt(15)
	v_add_f64 v[2:3], v[2:3], v[6:7]
	s_waitcnt vmcnt(14)
	v_add_f64 v[4:5], v[4:5], v[8:9]
	s_waitcnt vmcnt(13)
	v_add_f64 v[2:3], v[2:3], v[10:11]
	s_waitcnt vmcnt(12)
	v_add_f64 v[4:5], v[4:5], v[12:13]
	s_waitcnt vmcnt(11)
	v_add_f64 v[2:3], v[2:3], v[14:15]
	s_waitcnt vmcnt(10)
	v_add_f64 v[4:5], v[4:5], v[16:17]
	s_waitcnt vmcnt(9)
	v_add_f64 v[2:3], v[2:3], v[18:19]
	s_waitcnt vmcnt(8)
	v_add_f64 v[4:5], v[4:5], v[20:21]
	s_waitcnt vmcnt(7)
	v_add_f64 v[2:3], v[2:3], v[22:23]
	s_waitcnt vmcnt(6)
	v_add_f64 v[4:5], v[4:5], v[24:25]
	s_waitcnt vmcnt(5)
	v_add_f64 v[2:3], v[2:3], v[26:27]
	s_waitcnt vmcnt(4)
	v_add_f64 v[4:5], v[4:5], v[28:29]
	s_waitcnt vmcnt(3)
	v_add_f64 v[2:3], v[2:3], v[30:31]
	s_waitcnt vmcnt(2)
	v_add_f64 v[4:5], v[4:5], v[32:33]
	v_div_scale_f64 v[6:7], s[2:3], s[10:11], s[10:11], v[2:3]
	v_div_scale_f64 v[10:11], s[2:3], s[10:11], s[10:11], v[4:5]
	v_rcp_f64_e32 v[12:13], v[6:7]
	v_rcp_f64_e32 v[14:15], v[10:11]
	v_div_scale_f64 v[8:9], vcc, v[2:3], s[10:11], v[2:3]
	v_fma_f64 v[18:19], -v[6:7], v[12:13], 1.0
	v_fma_f64 v[20:21], -v[10:11], v[14:15], 1.0
	v_fmac_f64_e32 v[12:13], v[12:13], v[18:19]
	v_fmac_f64_e32 v[14:15], v[14:15], v[20:21]
	v_fma_f64 v[18:19], -v[6:7], v[12:13], 1.0
	v_fma_f64 v[20:21], -v[10:11], v[14:15], 1.0
	v_fmac_f64_e32 v[12:13], v[12:13], v[18:19]
	v_div_scale_f64 v[16:17], s[2:3], v[4:5], s[10:11], v[4:5]
	v_fmac_f64_e32 v[14:15], v[14:15], v[20:21]
	v_mul_f64 v[18:19], v[8:9], v[12:13]
	v_mul_f64 v[20:21], v[16:17], v[14:15]
	v_fma_f64 v[6:7], -v[6:7], v[18:19], v[8:9]
	v_fma_f64 v[8:9], -v[10:11], v[20:21], v[16:17]
	v_div_fmas_f64 v[6:7], v[6:7], v[12:13], v[18:19]
	s_mov_b64 vcc, s[2:3]
	v_div_fixup_f64 v[2:3], v[6:7], s[10:11], v[2:3]
	v_div_fmas_f64 v[6:7], v[8:9], v[14:15], v[20:21]
	v_div_fixup_f64 v[4:5], v[6:7], s[10:11], v[4:5]
	v_fma_f64 v[4:5], -v[2:3], v[2:3], v[4:5]
	v_cmp_ngt_f64_e32 vcc, 0, v[4:5]
	v_cvt_f32_f64_e32 v2, v[2:3]
	v_or_b32_e32 v18, s4, v1
	v_cndmask_b32_e32 v5, 0, v5, vcc
	v_cndmask_b32_e32 v4, 0, v4, vcc
	v_cvt_f32_f64_e32 v4, v[4:5]
	v_add_f32_e32 v4, 0x3727c5ac, v4
	v_mul_f32_e32 v5, 0x4b800000, v4
	v_cmp_gt_f32_e32 vcc, s5, v4
	s_nop 1
	v_cndmask_b32_e32 v4, v4, v5, vcc
	v_rsq_f32_e32 v4, v4
	s_nop 0
	v_mul_f32_e32 v3, 0x45800000, v4
	v_cndmask_b32_e32 v3, v4, v3, vcc
	s_waitcnt vmcnt(1)
	v_mul_f32_e32 v3, v3, v34
	s_waitcnt vmcnt(0)
	v_fma_f32 v2, -v3, v2, v35
	v_cmp_gt_i32_e32 vcc, s16, v18
	ds_write2st64_b32 v36, v3, v2 offset1:4
	s_waitcnt lgkmcnt(0)
	s_barrier
	s_load_dwordx2 s[2:3], s[0:1], 0x0
	s_load_dwordx4 s[12:15], s[0:1], 0x20
	s_and_b64 s[0:1], s[8:9], exec
	s_cselect_b32 s0, 0x186a000, 0
	v_and_b32_e32 v10, 63, v0
	v_lshrrev_b32_e32 v11, 6, v0
	v_lshlrev_b32_e32 v12, 4, v10
	ds_read_b128 v[2:5], v12
	ds_read_b128 v[6:9], v12 offset:1024
	v_lshlrev_b32_e32 v10, 3, v10
	v_readfirstlane_b32 s23, v11
	s_mov_b32 s28, 0x3c23d70a
	s_waitcnt lgkmcnt(0)
	s_add_u32 s2, s2, s0
	s_addc_u32 s3, s3, 0
	s_and_b64 s[20:21], s[8:9], exec
	s_cselect_b32 s21, s15, 0
	s_cselect_b32 s20, s14, 0
	s_lshl_b64 s[20:21], s[20:21], 2
	s_add_u32 s12, s12, s20
	s_addc_u32 s13, s13, s21
	s_add_i32 s23, s23, s4
	s_add_i32 s22, s23, 0
	s_min_i32 s22, s22, 0xc34f
	s_lshl_b32 s22, s22, 9
	s_add_u32 s24, s2, s22
	s_addc_u32 s25, s3, 0
	global_load_dwordx2 v[14:15], v10, s[24:25]
	s_add_i32 s22, s23, 4
	s_min_i32 s22, s22, 0xc34f
	s_lshl_b32 s22, s22, 9
	s_add_u32 s24, s2, s22
	s_addc_u32 s25, s3, 0
	global_load_dwordx2 v[16:17], v10, s[24:25]
	s_add_i32 s22, s23, 8
	s_min_i32 s22, s22, 0xc34f
	s_lshl_b32 s22, s22, 9
	s_add_u32 s24, s2, s22
	s_addc_u32 s25, s3, 0
	global_load_dwordx2 v[18:19], v10, s[24:25]
	s_add_i32 s22, s23, 12
	s_min_i32 s22, s22, 0xc34f
	s_lshl_b32 s22, s22, 9
	s_add_u32 s24, s2, s22
	s_addc_u32 s25, s3, 0
	global_load_dwordx2 v[20:21], v10, s[24:25]
	s_add_i32 s22, s23, 16
	s_min_i32 s22, s22, 0xc34f
	s_lshl_b32 s22, s22, 9
	s_add_u32 s24, s2, s22
	s_addc_u32 s25, s3, 0
	global_load_dwordx2 v[22:23], v10, s[24:25]
	s_add_i32 s22, s23, 20
	s_min_i32 s22, s22, 0xc34f
	s_lshl_b32 s22, s22, 9
	s_add_u32 s24, s2, s22
	s_addc_u32 s25, s3, 0
	global_load_dwordx2 v[24:25], v10, s[24:25]
	s_add_i32 s22, s23, 24
	s_min_i32 s22, s22, 0xc34f
	s_lshl_b32 s22, s22, 9
	s_add_u32 s24, s2, s22
	s_addc_u32 s25, s3, 0
	global_load_dwordx2 v[26:27], v10, s[24:25]
	s_add_i32 s22, s23, 28
	s_min_i32 s22, s22, 0xc34f
	s_lshl_b32 s22, s22, 9
	s_add_u32 s24, s2, s22
	s_addc_u32 s25, s3, 0
	global_load_dwordx2 v[28:29], v10, s[24:25]
	s_waitcnt vmcnt(7)
	v_cvt_f32_f16_sdwa v33, v14 dst_sel:DWORD dst_unused:UNUSED_PAD src0_sel:WORD_1
	v_cvt_f32_f16_e32 v32, v14
	v_cvt_f32_f16_sdwa v35, v15 dst_sel:DWORD dst_unused:UNUSED_PAD src0_sel:WORD_1
	v_cvt_f32_f16_e32 v34, v15
	v_pk_fma_f32 v[32:33], v[2:3], v[32:33], v[6:7]
	v_pk_fma_f32 v[34:35], v[4:5], v[34:35], v[8:9]
	v_pk_mul_f32 v[36:37], v[32:33], s[28:29] op_sel_hi:[1,0]
	v_pk_mul_f32 v[38:39], v[34:35], s[28:29] op_sel_hi:[1,0]
	v_cmp_lt_f32_e64 s[30:31], 0, v32
	v_cmp_lt_f32_e64 s[32:33], 0, v33
	v_cmp_lt_f32_e64 s[34:35], 0, v34
	v_cmp_lt_f32_e64 s[36:37], 0, v35
	v_cndmask_b32_e64 v32, v36, v32, s[30:31]
	v_cndmask_b32_e64 v33, v37, v33, s[32:33]
	v_cndmask_b32_e64 v34, v38, v34, s[34:35]
	v_cndmask_b32_e64 v35, v39, v35, s[36:37]
	s_add_i32 s22, s23, 0
	s_cmp_lt_i32 s22, s16
	s_cbranch_scc0 .Ln1_skip_0
	s_lshl_b32 s22, s22, 10
	s_add_u32 s26, s12, s22
	s_addc_u32 s27, s13, 0
	global_store_dwordx4 v12, v[32:35], s[26:27] sc1
.Ln1_skip_0:
	s_waitcnt vmcnt(7)
	v_cvt_f32_f16_sdwa v41, v16 dst_sel:DWORD dst_unused:UNUSED_PAD src0_sel:WORD_1
	v_cvt_f32_f16_e32 v40, v16
	v_cvt_f32_f16_sdwa v43, v17 dst_sel:DWORD dst_unused:UNUSED_PAD src0_sel:WORD_1
	v_cvt_f32_f16_e32 v42, v17
	v_pk_fma_f32 v[40:41], v[2:3], v[40:41], v[6:7]
	v_pk_fma_f32 v[42:43], v[4:5], v[42:43], v[8:9]
	v_pk_mul_f32 v[44:45], v[40:41], s[28:29] op_sel_hi:[1,0]
	v_pk_mul_f32 v[46:47], v[42:43], s[28:29] op_sel_hi:[1,0]
	v_cmp_lt_f32_e64 s[30:31], 0, v40
	v_cmp_lt_f32_e64 s[32:33], 0, v41
	v_cmp_lt_f32_e64 s[34:35], 0, v42
	v_cmp_lt_f32_e64 s[36:37], 0, v43
	v_cndmask_b32_e64 v40, v44, v40, s[30:31]
	v_cndmask_b32_e64 v41, v45, v41, s[32:33]
	v_cndmask_b32_e64 v42, v46, v42, s[34:35]
	v_cndmask_b32_e64 v43, v47, v43, s[36:37]
	s_add_i32 s22, s23, 4
	s_cmp_lt_i32 s22, s16
	s_cbranch_scc0 .Ln1_skip_1
	s_lshl_b32 s22, s22, 10
	s_add_u32 s26, s12, s22
	s_addc_u32 s27, s13, 0
	global_store_dwordx4 v12, v[40:43], s[26:27] sc1
.Ln1_skip_1:
	s_waitcnt vmcnt(7)
	v_cvt_f32_f16_sdwa v33, v18 dst_sel:DWORD dst_unused:UNUSED_PAD src0_sel:WORD_1
	v_cvt_f32_f16_e32 v32, v18
	v_cvt_f32_f16_sdwa v35, v19 dst_sel:DWORD dst_unused:UNUSED_PAD src0_sel:WORD_1
	v_cvt_f32_f16_e32 v34, v19
	v_pk_fma_f32 v[32:33], v[2:3], v[32:33], v[6:7]
	v_pk_fma_f32 v[34:35], v[4:5], v[34:35], v[8:9]
	v_pk_mul_f32 v[36:37], v[32:33], s[28:29] op_sel_hi:[1,0]
	v_pk_mul_f32 v[38:39], v[34:35], s[28:29] op_sel_hi:[1,0]
	v_cmp_lt_f32_e64 s[30:31], 0, v32
	v_cmp_lt_f32_e64 s[32:33], 0, v33
	v_cmp_lt_f32_e64 s[34:35], 0, v34
	v_cmp_lt_f32_e64 s[36:37], 0, v35
	v_cndmask_b32_e64 v32, v36, v32, s[30:31]
	v_cndmask_b32_e64 v33, v37, v33, s[32:33]
	v_cndmask_b32_e64 v34, v38, v34, s[34:35]
	v_cndmask_b32_e64 v35, v39, v35, s[36:37]
	s_add_i32 s22, s23, 8
	s_cmp_lt_i32 s22, s16
	s_cbranch_scc0 .Ln1_skip_2
	s_lshl_b32 s22, s22, 10
	s_add_u32 s26, s12, s22
	s_addc_u32 s27, s13, 0
	global_store_dwordx4 v12, v[32:35], s[26:27] sc1
.Ln1_skip_2:
	s_waitcnt vmcnt(7)
	v_cvt_f32_f16_sdwa v41, v20 dst_sel:DWORD dst_unused:UNUSED_PAD src0_sel:WORD_1
	v_cvt_f32_f16_e32 v40, v20
	v_cvt_f32_f16_sdwa v43, v21 dst_sel:DWORD dst_unused:UNUSED_PAD src0_sel:WORD_1
	v_cvt_f32_f16_e32 v42, v21
	v_pk_fma_f32 v[40:41], v[2:3], v[40:41], v[6:7]
	v_pk_fma_f32 v[42:43], v[4:5], v[42:43], v[8:9]
	v_pk_mul_f32 v[44:45], v[40:41], s[28:29] op_sel_hi:[1,0]
	v_pk_mul_f32 v[46:47], v[42:43], s[28:29] op_sel_hi:[1,0]
	v_cmp_lt_f32_e64 s[30:31], 0, v40
	v_cmp_lt_f32_e64 s[32:33], 0, v41
	v_cmp_lt_f32_e64 s[34:35], 0, v42
	v_cmp_lt_f32_e64 s[36:37], 0, v43
	v_cndmask_b32_e64 v40, v44, v40, s[30:31]
	v_cndmask_b32_e64 v41, v45, v41, s[32:33]
	v_cndmask_b32_e64 v42, v46, v42, s[34:35]
	v_cndmask_b32_e64 v43, v47, v43, s[36:37]
	s_add_i32 s22, s23, 12
	s_cmp_lt_i32 s22, s16
	s_cbranch_scc0 .Ln1_skip_3
	s_lshl_b32 s22, s22, 10
	s_add_u32 s26, s12, s22
	s_addc_u32 s27, s13, 0
	global_store_dwordx4 v12, v[40:43], s[26:27] sc1
.Ln1_skip_3:
	s_waitcnt vmcnt(7)
	v_cvt_f32_f16_sdwa v33, v22 dst_sel:DWORD dst_unused:UNUSED_PAD src0_sel:WORD_1
	v_cvt_f32_f16_e32 v32, v22
	v_cvt_f32_f16_sdwa v35, v23 dst_sel:DWORD dst_unused:UNUSED_PAD src0_sel:WORD_1
	v_cvt_f32_f16_e32 v34, v23
	v_pk_fma_f32 v[32:33], v[2:3], v[32:33], v[6:7]
	v_pk_fma_f32 v[34:35], v[4:5], v[34:35], v[8:9]
	v_pk_mul_f32 v[36:37], v[32:33], s[28:29] op_sel_hi:[1,0]
	v_pk_mul_f32 v[38:39], v[34:35], s[28:29] op_sel_hi:[1,0]
	v_cmp_lt_f32_e64 s[30:31], 0, v32
	v_cmp_lt_f32_e64 s[32:33], 0, v33
	v_cmp_lt_f32_e64 s[34:35], 0, v34
	v_cmp_lt_f32_e64 s[36:37], 0, v35
	v_cndmask_b32_e64 v32, v36, v32, s[30:31]
	v_cndmask_b32_e64 v33, v37, v33, s[32:33]
	v_cndmask_b32_e64 v34, v38, v34, s[34:35]
	v_cndmask_b32_e64 v35, v39, v35, s[36:37]
	s_add_i32 s22, s23, 16
	s_cmp_lt_i32 s22, s16
	s_cbranch_scc0 .Ln1_skip_4
	s_lshl_b32 s22, s22, 10
	s_add_u32 s26, s12, s22
	s_addc_u32 s27, s13, 0
	global_store_dwordx4 v12, v[32:35], s[26:27] sc1
.Ln1_skip_4:
	s_waitcnt vmcnt(7)
	v_cvt_f32_f16_sdwa v41, v24 dst_sel:DWORD dst_unused:UNUSED_PAD src0_sel:WORD_1
	v_cvt_f32_f16_e32 v40, v24
	v_cvt_f32_f16_sdwa v43, v25 dst_sel:DWORD dst_unused:UNUSED_PAD src0_sel:WORD_1
	v_cvt_f32_f16_e32 v42, v25
	v_pk_fma_f32 v[40:41], v[2:3], v[40:41], v[6:7]
	v_pk_fma_f32 v[42:43], v[4:5], v[42:43], v[8:9]
	v_pk_mul_f32 v[44:45], v[40:41], s[28:29] op_sel_hi:[1,0]
	v_pk_mul_f32 v[46:47], v[42:43], s[28:29] op_sel_hi:[1,0]
	v_cmp_lt_f32_e64 s[30:31], 0, v40
	v_cmp_lt_f32_e64 s[32:33], 0, v41
	v_cmp_lt_f32_e64 s[34:35], 0, v42
	v_cmp_lt_f32_e64 s[36:37], 0, v43
	v_cndmask_b32_e64 v40, v44, v40, s[30:31]
	v_cndmask_b32_e64 v41, v45, v41, s[32:33]
	v_cndmask_b32_e64 v42, v46, v42, s[34:35]
	v_cndmask_b32_e64 v43, v47, v43, s[36:37]
	s_add_i32 s22, s23, 20
	s_cmp_lt_i32 s22, s16
	s_cbranch_scc0 .Ln1_skip_5
	s_lshl_b32 s22, s22, 10
	s_add_u32 s26, s12, s22
	s_addc_u32 s27, s13, 0
	global_store_dwordx4 v12, v[40:43], s[26:27] sc1
.Ln1_skip_5:
	s_waitcnt vmcnt(7)
	v_cvt_f32_f16_sdwa v33, v26 dst_sel:DWORD dst_unused:UNUSED_PAD src0_sel:WORD_1
	v_cvt_f32_f16_e32 v32, v26
	v_cvt_f32_f16_sdwa v35, v27 dst_sel:DWORD dst_unused:UNUSED_PAD src0_sel:WORD_1
	v_cvt_f32_f16_e32 v34, v27
	v_pk_fma_f32 v[32:33], v[2:3], v[32:33], v[6:7]
	v_pk_fma_f32 v[34:35], v[4:5], v[34:35], v[8:9]
	v_pk_mul_f32 v[36:37], v[32:33], s[28:29] op_sel_hi:[1,0]
	v_pk_mul_f32 v[38:39], v[34:35], s[28:29] op_sel_hi:[1,0]
	v_cmp_lt_f32_e64 s[30:31], 0, v32
	v_cmp_lt_f32_e64 s[32:33], 0, v33
	v_cmp_lt_f32_e64 s[34:35], 0, v34
	v_cmp_lt_f32_e64 s[36:37], 0, v35
	v_cndmask_b32_e64 v32, v36, v32, s[30:31]
	v_cndmask_b32_e64 v33, v37, v33, s[32:33]
	v_cndmask_b32_e64 v34, v38, v34, s[34:35]
	v_cndmask_b32_e64 v35, v39, v35, s[36:37]
	s_add_i32 s22, s23, 24
	s_cmp_lt_i32 s22, s16
	s_cbranch_scc0 .Ln1_skip_6
	s_lshl_b32 s22, s22, 10
	s_add_u32 s26, s12, s22
	s_addc_u32 s27, s13, 0
	global_store_dwordx4 v12, v[32:35], s[26:27] sc1
.Ln1_skip_6:
	s_waitcnt vmcnt(7)
	v_cvt_f32_f16_sdwa v41, v28 dst_sel:DWORD dst_unused:UNUSED_PAD src0_sel:WORD_1
	v_cvt_f32_f16_e32 v40, v28
	v_cvt_f32_f16_sdwa v43, v29 dst_sel:DWORD dst_unused:UNUSED_PAD src0_sel:WORD_1
	v_cvt_f32_f16_e32 v42, v29
	v_pk_fma_f32 v[40:41], v[2:3], v[40:41], v[6:7]
	v_pk_fma_f32 v[42:43], v[4:5], v[42:43], v[8:9]
	v_pk_mul_f32 v[44:45], v[40:41], s[28:29] op_sel_hi:[1,0]
	v_pk_mul_f32 v[46:47], v[42:43], s[28:29] op_sel_hi:[1,0]
	v_cmp_lt_f32_e64 s[30:31], 0, v40
	v_cmp_lt_f32_e64 s[32:33], 0, v41
	v_cmp_lt_f32_e64 s[34:35], 0, v42
	v_cmp_lt_f32_e64 s[36:37], 0, v43
	v_cndmask_b32_e64 v40, v44, v40, s[30:31]
	v_cndmask_b32_e64 v41, v45, v41, s[32:33]
	v_cndmask_b32_e64 v42, v46, v42, s[34:35]
	v_cndmask_b32_e64 v43, v47, v43, s[36:37]
	s_add_i32 s22, s23, 28
	s_cmp_lt_i32 s22, s16
	s_cbranch_scc0 .Ln1_skip_7
	s_lshl_b32 s22, s22, 10
	s_add_u32 s26, s12, s22
	s_addc_u32 s27, s13, 0
	global_store_dwordx4 v12, v[40:43], s[26:27] sc1
.Ln1_skip_7:
	s_add_i32 s22, s23, 32
	s_min_i32 s22, s22, 0xc34f
	s_lshl_b32 s22, s22, 9
	s_add_u32 s24, s2, s22
	s_addc_u32 s25, s3, 0
	global_load_dwordx2 v[14:15], v10, s[24:25]
	s_add_i32 s22, s23, 36
	s_min_i32 s22, s22, 0xc34f
	s_lshl_b32 s22, s22, 9
	s_add_u32 s24, s2, s22
	s_addc_u32 s25, s3, 0
	global_load_dwordx2 v[16:17], v10, s[24:25]
	s_add_i32 s22, s23, 40
	s_min_i32 s22, s22, 0xc34f
	s_lshl_b32 s22, s22, 9
	s_add_u32 s24, s2, s22
	s_addc_u32 s25, s3, 0
	global_load_dwordx2 v[18:19], v10, s[24:25]
	s_add_i32 s22, s23, 44
	s_min_i32 s22, s22, 0xc34f
	s_lshl_b32 s22, s22, 9
	s_add_u32 s24, s2, s22
	s_addc_u32 s25, s3, 0
	global_load_dwordx2 v[20:21], v10, s[24:25]
	s_add_i32 s22, s23, 48
	s_min_i32 s22, s22, 0xc34f
	s_lshl_b32 s22, s22, 9
	s_add_u32 s24, s2, s22
	s_addc_u32 s25, s3, 0
	global_load_dwordx2 v[22:23], v10, s[24:25]
	s_add_i32 s22, s23, 52
	s_min_i32 s22, s22, 0xc34f
	s_lshl_b32 s22, s22, 9
	s_add_u32 s24, s2, s22
	s_addc_u32 s25, s3, 0
	global_load_dwordx2 v[24:25], v10, s[24:25]
	s_add_i32 s22, s23, 56
	s_min_i32 s22, s22, 0xc34f
	s_lshl_b32 s22, s22, 9
	s_add_u32 s24, s2, s22
	s_addc_u32 s25, s3, 0
	global_load_dwordx2 v[26:27], v10, s[24:25]
	s_add_i32 s22, s23, 60
	s_min_i32 s22, s22, 0xc34f
	s_lshl_b32 s22, s22, 9
	s_add_u32 s24, s2, s22
	s_addc_u32 s25, s3, 0
	global_load_dwordx2 v[28:29], v10, s[24:25]
	s_waitcnt vmcnt(7)
	v_cvt_f32_f16_sdwa v33, v14 dst_sel:DWORD dst_unused:UNUSED_PAD src0_sel:WORD_1
	v_cvt_f32_f16_e32 v32, v14
	v_cvt_f32_f16_sdwa v35, v15 dst_sel:DWORD dst_unused:UNUSED_PAD src0_sel:WORD_1
	v_cvt_f32_f16_e32 v34, v15
	v_pk_fma_f32 v[32:33], v[2:3], v[32:33], v[6:7]
	v_pk_fma_f32 v[34:35], v[4:5], v[34:35], v[8:9]
	v_pk_mul_f32 v[36:37], v[32:33], s[28:29] op_sel_hi:[1,0]
	v_pk_mul_f32 v[38:39], v[34:35], s[28:29] op_sel_hi:[1,0]
	v_cmp_lt_f32_e64 s[30:31], 0, v32
	v_cmp_lt_f32_e64 s[32:33], 0, v33
	v_cmp_lt_f32_e64 s[34:35], 0, v34
	v_cmp_lt_f32_e64 s[36:37], 0, v35
	v_cndmask_b32_e64 v32, v36, v32, s[30:31]
	v_cndmask_b32_e64 v33, v37, v33, s[32:33]
	v_cndmask_b32_e64 v34, v38, v34, s[34:35]
	v_cndmask_b32_e64 v35, v39, v35, s[36:37]
	s_add_i32 s22, s23, 32
	s_cmp_lt_i32 s22, s16
	s_cbranch_scc0 .Ln1_skip_8
	s_lshl_b32 s22, s22, 10
	s_add_u32 s26, s12, s22
	s_addc_u32 s27, s13, 0
	global_store_dwordx4 v12, v[32:35], s[26:27] sc1
.Ln1_skip_8:
	s_waitcnt vmcnt(7)
	v_cvt_f32_f16_sdwa v41, v16 dst_sel:DWORD dst_unused:UNUSED_PAD src0_sel:WORD_1
	v_cvt_f32_f16_e32 v40, v16
	v_cvt_f32_f16_sdwa v43, v17 dst_sel:DWORD dst_unused:UNUSED_PAD src0_sel:WORD_1
	v_cvt_f32_f16_e32 v42, v17
	v_pk_fma_f32 v[40:41], v[2:3], v[40:41], v[6:7]
	v_pk_fma_f32 v[42:43], v[4:5], v[42:43], v[8:9]
	v_pk_mul_f32 v[44:45], v[40:41], s[28:29] op_sel_hi:[1,0]
	v_pk_mul_f32 v[46:47], v[42:43], s[28:29] op_sel_hi:[1,0]
	v_cmp_lt_f32_e64 s[30:31], 0, v40
	v_cmp_lt_f32_e64 s[32:33], 0, v41
	v_cmp_lt_f32_e64 s[34:35], 0, v42
	v_cmp_lt_f32_e64 s[36:37], 0, v43
	v_cndmask_b32_e64 v40, v44, v40, s[30:31]
	v_cndmask_b32_e64 v41, v45, v41, s[32:33]
	v_cndmask_b32_e64 v42, v46, v42, s[34:35]
	v_cndmask_b32_e64 v43, v47, v43, s[36:37]
	s_add_i32 s22, s23, 36
	s_cmp_lt_i32 s22, s16
	s_cbranch_scc0 .Ln1_skip_9
	s_lshl_b32 s22, s22, 10
	s_add_u32 s26, s12, s22
	s_addc_u32 s27, s13, 0
	global_store_dwordx4 v12, v[40:43], s[26:27] sc1
.Ln1_skip_9:
	s_waitcnt vmcnt(7)
	v_cvt_f32_f16_sdwa v33, v18 dst_sel:DWORD dst_unused:UNUSED_PAD src0_sel:WORD_1
	v_cvt_f32_f16_e32 v32, v18
	v_cvt_f32_f16_sdwa v35, v19 dst_sel:DWORD dst_unused:UNUSED_PAD src0_sel:WORD_1
	v_cvt_f32_f16_e32 v34, v19
	v_pk_fma_f32 v[32:33], v[2:3], v[32:33], v[6:7]
	v_pk_fma_f32 v[34:35], v[4:5], v[34:35], v[8:9]
	v_pk_mul_f32 v[36:37], v[32:33], s[28:29] op_sel_hi:[1,0]
	v_pk_mul_f32 v[38:39], v[34:35], s[28:29] op_sel_hi:[1,0]
	v_cmp_lt_f32_e64 s[30:31], 0, v32
	v_cmp_lt_f32_e64 s[32:33], 0, v33
	v_cmp_lt_f32_e64 s[34:35], 0, v34
	v_cmp_lt_f32_e64 s[36:37], 0, v35
	v_cndmask_b32_e64 v32, v36, v32, s[30:31]
	v_cndmask_b32_e64 v33, v37, v33, s[32:33]
	v_cndmask_b32_e64 v34, v38, v34, s[34:35]
	v_cndmask_b32_e64 v35, v39, v35, s[36:37]
	s_add_i32 s22, s23, 40
	s_cmp_lt_i32 s22, s16
	s_cbranch_scc0 .Ln1_skip_10
	s_lshl_b32 s22, s22, 10
	s_add_u32 s26, s12, s22
	s_addc_u32 s27, s13, 0
	global_store_dwordx4 v12, v[32:35], s[26:27] sc1
.Ln1_skip_10:
	s_waitcnt vmcnt(7)
	v_cvt_f32_f16_sdwa v41, v20 dst_sel:DWORD dst_unused:UNUSED_PAD src0_sel:WORD_1
	v_cvt_f32_f16_e32 v40, v20
	v_cvt_f32_f16_sdwa v43, v21 dst_sel:DWORD dst_unused:UNUSED_PAD src0_sel:WORD_1
	v_cvt_f32_f16_e32 v42, v21
	v_pk_fma_f32 v[40:41], v[2:3], v[40:41], v[6:7]
	v_pk_fma_f32 v[42:43], v[4:5], v[42:43], v[8:9]
	v_pk_mul_f32 v[44:45], v[40:41], s[28:29] op_sel_hi:[1,0]
	v_pk_mul_f32 v[46:47], v[42:43], s[28:29] op_sel_hi:[1,0]
	v_cmp_lt_f32_e64 s[30:31], 0, v40
	v_cmp_lt_f32_e64 s[32:33], 0, v41
	v_cmp_lt_f32_e64 s[34:35], 0, v42
	v_cmp_lt_f32_e64 s[36:37], 0, v43
	v_cndmask_b32_e64 v40, v44, v40, s[30:31]
	v_cndmask_b32_e64 v41, v45, v41, s[32:33]
	v_cndmask_b32_e64 v42, v46, v42, s[34:35]
	v_cndmask_b32_e64 v43, v47, v43, s[36:37]
	s_add_i32 s22, s23, 44
	s_cmp_lt_i32 s22, s16
	s_cbranch_scc0 .Ln1_skip_11
	s_lshl_b32 s22, s22, 10
	s_add_u32 s26, s12, s22
	s_addc_u32 s27, s13, 0
	global_store_dwordx4 v12, v[40:43], s[26:27] sc1
.Ln1_skip_11:
	s_waitcnt vmcnt(7)
	v_cvt_f32_f16_sdwa v33, v22 dst_sel:DWORD dst_unused:UNUSED_PAD src0_sel:WORD_1
	v_cvt_f32_f16_e32 v32, v22
	v_cvt_f32_f16_sdwa v35, v23 dst_sel:DWORD dst_unused:UNUSED_PAD src0_sel:WORD_1
	v_cvt_f32_f16_e32 v34, v23
	v_pk_fma_f32 v[32:33], v[2:3], v[32:33], v[6:7]
	v_pk_fma_f32 v[34:35], v[4:5], v[34:35], v[8:9]
	v_pk_mul_f32 v[36:37], v[32:33], s[28:29] op_sel_hi:[1,0]
	v_pk_mul_f32 v[38:39], v[34:35], s[28:29] op_sel_hi:[1,0]
	v_cmp_lt_f32_e64 s[30:31], 0, v32
	v_cmp_lt_f32_e64 s[32:33], 0, v33
	v_cmp_lt_f32_e64 s[34:35], 0, v34
	v_cmp_lt_f32_e64 s[36:37], 0, v35
	v_cndmask_b32_e64 v32, v36, v32, s[30:31]
	v_cndmask_b32_e64 v33, v37, v33, s[32:33]
	v_cndmask_b32_e64 v34, v38, v34, s[34:35]
	v_cndmask_b32_e64 v35, v39, v35, s[36:37]
	s_add_i32 s22, s23, 48
	s_cmp_lt_i32 s22, s16
	s_cbranch_scc0 .Ln1_skip_12
	s_lshl_b32 s22, s22, 10
	s_add_u32 s26, s12, s22
	s_addc_u32 s27, s13, 0
	global_store_dwordx4 v12, v[32:35], s[26:27] sc1
.Ln1_skip_12:
	s_waitcnt vmcnt(7)
	v_cvt_f32_f16_sdwa v41, v24 dst_sel:DWORD dst_unused:UNUSED_PAD src0_sel:WORD_1
	v_cvt_f32_f16_e32 v40, v24
	v_cvt_f32_f16_sdwa v43, v25 dst_sel:DWORD dst_unused:UNUSED_PAD src0_sel:WORD_1
	v_cvt_f32_f16_e32 v42, v25
	v_pk_fma_f32 v[40:41], v[2:3], v[40:41], v[6:7]
	v_pk_fma_f32 v[42:43], v[4:5], v[42:43], v[8:9]
	v_pk_mul_f32 v[44:45], v[40:41], s[28:29] op_sel_hi:[1,0]
	v_pk_mul_f32 v[46:47], v[42:43], s[28:29] op_sel_hi:[1,0]
	v_cmp_lt_f32_e64 s[30:31], 0, v40
	v_cmp_lt_f32_e64 s[32:33], 0, v41
	v_cmp_lt_f32_e64 s[34:35], 0, v42
	v_cmp_lt_f32_e64 s[36:37], 0, v43
	v_cndmask_b32_e64 v40, v44, v40, s[30:31]
	v_cndmask_b32_e64 v41, v45, v41, s[32:33]
	v_cndmask_b32_e64 v42, v46, v42, s[34:35]
	v_cndmask_b32_e64 v43, v47, v43, s[36:37]
	s_add_i32 s22, s23, 52
	s_cmp_lt_i32 s22, s16
	s_cbranch_scc0 .Ln1_skip_13
	s_lshl_b32 s22, s22, 10
	s_add_u32 s26, s12, s22
	s_addc_u32 s27, s13, 0
	global_store_dwordx4 v12, v[40:43], s[26:27] sc1
.Ln1_skip_13:
	s_waitcnt vmcnt(7)
	v_cvt_f32_f16_sdwa v33, v26 dst_sel:DWORD dst_unused:UNUSED_PAD src0_sel:WORD_1
	v_cvt_f32_f16_e32 v32, v26
	v_cvt_f32_f16_sdwa v35, v27 dst_sel:DWORD dst_unused:UNUSED_PAD src0_sel:WORD_1
	v_cvt_f32_f16_e32 v34, v27
	v_pk_fma_f32 v[32:33], v[2:3], v[32:33], v[6:7]
	v_pk_fma_f32 v[34:35], v[4:5], v[34:35], v[8:9]
	v_pk_mul_f32 v[36:37], v[32:33], s[28:29] op_sel_hi:[1,0]
	v_pk_mul_f32 v[38:39], v[34:35], s[28:29] op_sel_hi:[1,0]
	v_cmp_lt_f32_e64 s[30:31], 0, v32
	v_cmp_lt_f32_e64 s[32:33], 0, v33
	v_cmp_lt_f32_e64 s[34:35], 0, v34
	v_cmp_lt_f32_e64 s[36:37], 0, v35
	v_cndmask_b32_e64 v32, v36, v32, s[30:31]
	v_cndmask_b32_e64 v33, v37, v33, s[32:33]
	v_cndmask_b32_e64 v34, v38, v34, s[34:35]
	v_cndmask_b32_e64 v35, v39, v35, s[36:37]
	s_add_i32 s22, s23, 56
	s_cmp_lt_i32 s22, s16
	s_cbranch_scc0 .Ln1_skip_14
	s_lshl_b32 s22, s22, 10
	s_add_u32 s26, s12, s22
	s_addc_u32 s27, s13, 0
	global_store_dwordx4 v12, v[32:35], s[26:27] sc1
.Ln1_skip_14:
	s_waitcnt vmcnt(7)
	v_cvt_f32_f16_sdwa v41, v28 dst_sel:DWORD dst_unused:UNUSED_PAD src0_sel:WORD_1
	v_cvt_f32_f16_e32 v40, v28
	v_cvt_f32_f16_sdwa v43, v29 dst_sel:DWORD dst_unused:UNUSED_PAD src0_sel:WORD_1
	v_cvt_f32_f16_e32 v42, v29
	v_pk_fma_f32 v[40:41], v[2:3], v[40:41], v[6:7]
	v_pk_fma_f32 v[42:43], v[4:5], v[42:43], v[8:9]
	v_pk_mul_f32 v[44:45], v[40:41], s[28:29] op_sel_hi:[1,0]
	v_pk_mul_f32 v[46:47], v[42:43], s[28:29] op_sel_hi:[1,0]
	v_cmp_lt_f32_e64 s[30:31], 0, v40
	v_cmp_lt_f32_e64 s[32:33], 0, v41
	v_cmp_lt_f32_e64 s[34:35], 0, v42
	v_cmp_lt_f32_e64 s[36:37], 0, v43
	v_cndmask_b32_e64 v40, v44, v40, s[30:31]
	v_cndmask_b32_e64 v41, v45, v41, s[32:33]
	v_cndmask_b32_e64 v42, v46, v42, s[34:35]
	v_cndmask_b32_e64 v43, v47, v43, s[36:37]
	s_add_i32 s22, s23, 60
	s_cmp_lt_i32 s22, s16
	s_cbranch_scc0 .Ln1_skip_15
	s_lshl_b32 s22, s22, 10
	s_add_u32 s26, s12, s22
	s_addc_u32 s27, s13, 0
	global_store_dwordx4 v12, v[40:43], s[26:27] sc1
.Ln1_skip_15:
.LBB7_17:
	s_endpgm
	.p2alignl 8, 3212836864

	.amdhsa_kernel _Z6k_normILb1EEvPKDF16_PKdPKfS5_Pvm
		.amdhsa_group_segment_fixed_size 2048
		.amdhsa_private_segment_fixed_size 0
		.amdhsa_kernarg_size 48
		.amdhsa_user_sgpr_count 2
		.amdhsa_user_sgpr_dispatch_ptr 0
		.amdhsa_user_sgpr_queue_ptr 0
		.amdhsa_user_sgpr_kernarg_segment_ptr 1
		.amdhsa_user_sgpr_dispatch_id 0
		.amdhsa_user_sgpr_kernarg_preload_length 0
		.amdhsa_user_sgpr_kernarg_preload_offset 0
		.amdhsa_user_sgpr_private_segment_size 0
		.amdhsa_uses_dynamic_stack 0
		.amdhsa_enable_private_segment 0
		.amdhsa_system_sgpr_workgroup_id_x 1
		.amdhsa_system_sgpr_workgroup_id_y 0
		.amdhsa_system_sgpr_workgroup_id_z 0
		.amdhsa_system_sgpr_workgroup_info 0
		.amdhsa_system_vgpr_workitem_id 0
		.amdhsa_next_free_vgpr 52
		.amdhsa_next_free_sgpr 40
		.amdhsa_accum_offset 52
		.amdhsa_reserve_vcc 1
		.amdhsa_float_round_mode_32 0
		.amdhsa_float_round_mode_16_64 0
		.amdhsa_float_denorm_mode_32 3
		.amdhsa_float_denorm_mode_16_64 3
		.amdhsa_dx10_clamp 1
		.amdhsa_ieee_mode 1
		.amdhsa_fp16_overflow 0
		.amdhsa_tg_split 0
		.amdhsa_exception_fp_ieee_invalid_op 0
		.amdhsa_exception_fp_denorm_src 0
		.amdhsa_exception_fp_ieee_div_zero 0
		.amdhsa_exception_fp_ieee_overflow 0
		.amdhsa_exception_fp_ieee_underflow 0
		.amdhsa_exception_fp_ieee_inexact 0
		.amdhsa_exception_int_div_zero 0
	.end_amdhsa_kernel

amdhsa.kernels:
  - .agpr_count:     0
    .args:
      - .offset:         0
        .size:           336
        .value_kind:     by_value
    .group_segment_fixed_size: 1024
    .kernarg_segment_align: 8
    .kernarg_segment_size: 336
    .language:       OpenCL C
    .language_version:
      - 2
      - 0
    .max_flat_workgroup_size: 256
    .name:           _Z6k_prep8PrepArgs
    .private_segment_fixed_size: 0
    .sgpr_count:     30
    .sgpr_spill_count: 0
    .symbol:         _Z6k_prep8PrepArgs.kd
    .uniform_work_group_size: 1
    .uses_dynamic_stack: false
    .vgpr_count:     20
    .vgpr_spill_count: 0
    .wavefront_size: 64
  - .agpr_count:     0
    .args:
      - .address_space:  global
        .offset:         0
        .size:           8
        .value_kind:     global_buffer
      - .actual_access:  write_only
        .address_space:  global
        .offset:         8
        .size:           8
        .value_kind:     global_buffer
    .group_segment_fixed_size: 16
    .kernarg_segment_align: 8
    .kernarg_segment_size: 16
    .language:       OpenCL C
    .language_version:
      - 2
      - 0
    .max_flat_workgroup_size: 256
    .name:           _Z7k_bscanPiS_
    .private_segment_fixed_size: 0
    .sgpr_count:     22
    .sgpr_spill_count: 0
    .symbol:         _Z7k_bscanPiS_.kd
    .uniform_work_group_size: 1
    .uses_dynamic_stack: false
    .vgpr_count:     18
    .vgpr_spill_count: 0
    .wavefront_size: 64
  - .agpr_count:     16
    .args:
      - .offset:         0
        .size:           24
        .value_kind:     by_value
      - .actual_access:  read_only
        .address_space:  global
        .offset:         24
        .size:           8
        .value_kind:     global_buffer
      - .actual_access:  read_only
        .address_space:  global
        .offset:         32
        .size:           8
        .value_kind:     global_buffer
      - .actual_access:  write_only
        .address_space:  global
        .offset:         40
        .size:           8
        .value_kind:     global_buffer
      - .offset:         48
        .size:           608
        .value_kind:     by_value
      - .actual_access:  read_only
        .address_space:  global
        .offset:         656
        .size:           8
        .value_kind:     global_buffer
      - .actual_access:  write_only
        .address_space:  global
        .offset:         664
        .size:           8
        .value_kind:     global_buffer
    .group_segment_fixed_size: 33024
    .kernarg_segment_align: 8
    .kernarg_segment_size: 672
    .language:       OpenCL C
    .language_version:
      - 2
      - 0
    .max_flat_workgroup_size: 256
    .name:           _Z9k_scatter8EdgePtrsPKiS1_Pj8FoldArgsPKfPDF16_
    .private_segment_fixed_size: 0
    .sgpr_count:     28
    .sgpr_spill_count: 0
    .symbol:         _Z9k_scatter8EdgePtrsPKiS1_Pj8FoldArgsPKfPDF16_.kd
    .uniform_work_group_size: 1
    .uses_dynamic_stack: false
    .vgpr_count:     116
    .vgpr_spill_count: 0
    .wavefront_size: 64
  - .agpr_count:     0
    .args:
      - .actual_access:  read_only
        .address_space:  global
        .offset:         0
        .size:           8
        .value_kind:     global_buffer
      - .actual_access:  read_only
        .address_space:  global
        .offset:         8
        .size:           8
        .value_kind:     global_buffer
      - .actual_access:  write_only
        .address_space:  global
        .offset:         16
        .size:           8
        .value_kind:     global_buffer
      - .actual_access:  write_only
        .address_space:  global
        .offset:         24
        .size:           8
        .value_kind:     global_buffer
      - .actual_access:  read_only
        .address_space:  global
        .offset:         32
        .size:           8
        .value_kind:     global_buffer
      - .actual_access:  write_only
        .address_space:  global
        .offset:         40
        .size:           8
        .value_kind:     global_buffer
    .group_segment_fixed_size: 1048
    .kernarg_segment_align: 8
    .kernarg_segment_size: 48
    .language:       OpenCL C
    .language_version:
      - 2
      - 0
    .max_flat_workgroup_size: 256
    .name:           _Z6k_finePKiPKjPiPtPKfPDF16_
    .private_segment_fixed_size: 0
    .sgpr_count:     47
    .sgpr_spill_count: 0
    .symbol:         _Z6k_finePKiPKjPiPtPKfPDF16_.kd
    .uniform_work_group_size: 1
    .uses_dynamic_stack: false
    .vgpr_count:     28
    .vgpr_spill_count: 0
    .wavefront_size: 64
  - .agpr_count:     0
    .args:
      - .offset:         0
        .size:           40
        .value_kind:     by_value
      - .offset:         40
        .size:           40
        .value_kind:     by_value
      - .offset:         80
        .size:           40
        .value_kind:     by_value
    .group_segment_fixed_size: 0
    .kernarg_segment_align: 8
    .kernarg_segment_size: 120
    .language:       OpenCL C
    .language_version:
      - 2
      - 0
    .max_flat_workgroup_size: 256
    .name:           _Z5k_agg6AggJobS_S_
    .private_segment_fixed_size: 0
    .sgpr_count:     34
    .sgpr_spill_count: 0
    .symbol:         _Z5k_agg6AggJobS_S_.kd
    .uniform_work_group_size: 1
    .uses_dynamic_stack: false
    .vgpr_count:     60
    .vgpr_spill_count: 0
    .wavefront_size: 64
  - .agpr_count:     0
    .args:
      - .offset:         0
        .size:           48
        .value_kind:     by_value
      - .offset:         48
        .size:           48
        .value_kind:     by_value
    .group_segment_fixed_size: 0
    .kernarg_segment_align: 8
    .kernarg_segment_size: 96
    .language:       OpenCL C
    .language_version:
      - 2
      - 0
    .max_flat_workgroup_size: 512
    .name:           _Z6k_gemm8GemmProbS_
    .private_segment_fixed_size: 0
    .sgpr_count:     100
    .sgpr_spill_count: 0
    .symbol:         _Z6k_gemm8GemmProbS_.kd
    .uniform_work_group_size: 1
    .uses_dynamic_stack: false
    .vgpr_count:     240
    .vgpr_spill_count: 0
    .wavefront_size: 64
  - .agpr_count:     0
    .args:
      - .actual_access:  read_only
        .address_space:  global
        .offset:         0
        .size:           8
        .value_kind:     global_buffer
      - .actual_access:  read_only
        .address_space:  global
        .offset:         8
        .size:           8
        .value_kind:     global_buffer
      - .actual_access:  read_only
        .address_space:  global
        .offset:         16
        .size:           8
        .value_kind:     global_buffer
      - .actual_access:  read_only
        .address_space:  global
        .offset:         24
        .size:           8
        .value_kind:     global_buffer
      - .actual_access:  write_only
        .address_space:  global
        .offset:         32
        .size:           8
        .value_kind:     global_buffer
      - .offset:         40
        .size:           8
        .value_kind:     by_value
    .group_segment_fixed_size: 2048
    .kernarg_segment_align: 8
    .kernarg_segment_size: 48
    .language:       OpenCL C
    .language_version:
      - 2
      - 0
    .max_flat_workgroup_size: 256
    .name:           _Z6k_normILb0EEvPKDF16_PKdPKfS5_Pvm
    .private_segment_fixed_size: 0
    .sgpr_count:     23
    .sgpr_spill_count: 0
    .symbol:         _Z6k_normILb0EEvPKDF16_PKdPKfS5_Pvm.kd
    .uniform_work_group_size: 1
    .uses_dynamic_stack: false
    .vgpr_count:     56
    .vgpr_spill_count: 0
    .wavefront_size: 64
  - .agpr_count:     0
    .args:
      - .actual_access:  read_only
        .address_space:  global
        .offset:         0
        .size:           8
        .value_kind:     global_buffer
      - .actual_access:  read_only
        .address_space:  global
        .offset:         8
        .size:           8
        .value_kind:     global_buffer
      - .actual_access:  read_only
        .address_space:  global
        .offset:         16
        .size:           8
        .value_kind:     global_buffer
      - .actual_access:  read_only
        .address_space:  global
        .offset:         24
        .size:           8
        .value_kind:     global_buffer
      - .actual_access:  write_only
        .address_space:  global
        .offset:         32
        .size:           8
        .value_kind:     global_buffer
      - .offset:         40
        .size:           8
        .value_kind:     by_value
    .group_segment_fixed_size: 2048
    .kernarg_segment_align: 8
    .kernarg_segment_size: 48
    .language:       OpenCL C
    .language_version:
      - 2
      - 0
    .max_flat_workgroup_size: 256
    .name:           _Z6k_normILb1EEvPKDF16_PKdPKfS5_Pvm
    .private_segment_fixed_size: 0
    .sgpr_count:     46
    .sgpr_spill_count: 0
    .symbol:         _Z6k_normILb1EEvPKDF16_PKdPKfS5_Pvm.kd
    .uniform_work_group_size: 1
    .uses_dynamic_stack: false
    .vgpr_count:     52
    .vgpr_spill_count: 0
    .wavefront_size: 64
